# pool2: LDS float atomics replaced by exact f32 read/add/compare-and-swap loops (ds_add_f32 is ~7x slower than integer LDS atomics here)
# speedup vs baseline: 1.0237x; 1.0237x over previous
.Lp2_cas_s0:
	ds_read_b32 v124, v88
	s_waitcnt lgkmcnt(0)
	v_add_f32_e32 v125, v124, v86
	ds_cmpst_rtn_b32 v89, v88, v124, v125
	s_waitcnt lgkmcnt(0)
	v_cmp_ne_u32_e32 vcc, v89, v124
	s_and_b64 exec, exec, vcc
	s_cbranch_execnz .Lp2_cas_s0

.Lp2_cas_s1:
	ds_read_b32 v84, v83
	s_waitcnt lgkmcnt(0)
	v_add_f32_e32 v85, v84, v82
	ds_cmpst_rtn_b32 v86, v83, v84, v85
	s_waitcnt lgkmcnt(0)
	v_cmp_ne_u32_e32 vcc, v86, v84
	s_and_b64 exec, exec, vcc
	s_cbranch_execnz .Lp2_cas_s1

.Lp2_cas_s2:
	ds_read_b32 v80, v79
	s_waitcnt lgkmcnt(0)
	v_add_f32_e32 v81, v80, v78
	ds_cmpst_rtn_b32 v86, v79, v80, v81
	s_waitcnt lgkmcnt(0)
	v_cmp_ne_u32_e32 vcc, v86, v80
	s_and_b64 exec, exec, vcc
	s_cbranch_execnz .Lp2_cas_s2

.Lp2_cas_s3:
	ds_read_b32 v76, v75
	s_waitcnt lgkmcnt(0)
	v_add_f32_e32 v77, v76, v74
	ds_cmpst_rtn_b32 v86, v75, v76, v77
	s_waitcnt lgkmcnt(0)
	v_cmp_ne_u32_e32 vcc, v86, v76
	s_and_b64 exec, exec, vcc
	s_cbranch_execnz .Lp2_cas_s3

.Lp2_cas_s4:
	ds_read_b32 v72, v71
	s_waitcnt lgkmcnt(0)
	v_add_f32_e32 v73, v72, v70
	ds_cmpst_rtn_b32 v86, v71, v72, v73
	s_waitcnt lgkmcnt(0)
	v_cmp_ne_u32_e32 vcc, v86, v72
	s_and_b64 exec, exec, vcc
	s_cbranch_execnz .Lp2_cas_s4
	s_branch .LBB4_22

.Lp2_cas_self:
	ds_read_b32 v68, v67
	s_waitcnt lgkmcnt(0)
	v_add_f32_e32 v69, v68, v66
	ds_cmpst_rtn_b32 v70, v67, v68, v69
	s_waitcnt lgkmcnt(0)
	v_cmp_ne_u32_e32 vcc, v70, v68
	s_and_b64 exec, exec, vcc
	s_cbranch_execnz .Lp2_cas_self
